# speedup vs baseline: 1.0158x; 1.0158x over previous
_Z12oproj_kernelPKDF16_S0_PKfPf:
	s_load_dwordx8 s[4:11], s[0:1], 0x0
	s_lshl_b32 s0, s2, 2
	s_lshr_b32 s1, s2, 6
	s_and_b32 s0, s0, 28
	s_add_i32 s0, s0, s1
	v_bfe_u32 v14, v0, 6, 1
	s_bfe_u32 s13, s2, 0x30003
	s_lshl_b32 s12, s0, 7
	s_mul_i32 s0, s0, 0x44000
	v_bfe_u32 v12, v0, 4, 2
	v_and_b32_e32 v1, 7, v0
	v_lshlrev_b32_e32 v2, 2, v14
	s_mul_hi_i32 s1, s12, 0x880
	s_waitcnt lgkmcnt(0)
	s_add_u32 s0, s4, s0
	v_lshrrev_b32_e32 v13, 6, v0
	v_bitop3_b32 v1, v2, v1, v12 bitop3:0x36
	v_bfe_u32 v2, v0, 3, 3
	s_addc_u32 s1, s5, s1
	s_mul_i32 s2, s13, 0x44000
	v_lshl_or_b32 v2, v13, 3, v2
	s_add_u32 s2, s6, s2
	v_mul_u32_u24_e32 v2, 0x440, v2
	s_addc_u32 s3, s7, 0
	v_readfirstlane_b32 s27, v13
	s_nop 3
	s_cmp_lt_u32 s27, 4
	s_cbranch_scc0 .Lop_noprio
	s_setprio 1
.Lop_noprio:
	v_lshlrev_b32_e32 v2, 1, v2
	v_mov_b32_e32 v3, 0
	v_lshl_add_u64 v[4:5], s[0:1], 0, v[2:3]
	v_lshl_add_u64 v[10:11], s[2:3], 0, v[2:3]
	v_bfe_u32 v2, v0, 1, 3
	v_and_b32_e32 v9, 15, v0
	v_lshlrev_b32_e32 v6, 4, v1
	v_mov_b32_e32 v7, v3
	v_xor_b32_e32 v17, v12, v2
	v_bitop3_b32 v38, v12, v2, 4 bitop3:0x36
	v_lshlrev_b32_e32 v2, 10, v13
	v_lshl_add_u64 v[4:5], v[4:5], 0, v[6:7]
	v_lshl_add_u64 v[6:7], v[10:11], 0, v[6:7]
	v_lshlrev_b32_e32 v10, 7, v9
	v_add_u32_e32 v94, 0, v2
	s_mov_b64 s[0:1], 0x22000
	s_mov_b64 s[14:15], src_shared_base
	v_lshl_or_b32 v62, v14, 13, v10
	v_lshl_add_u64 v[10:11], v[4:5], 0, s[0:1]
	v_lshl_add_u64 v[12:13], v[6:7], 0, s[0:1]
	v_readfirstlane_b32 s22, v94
	s_mov_b32 s0, m0
	s_mov_b32 m0, s22
	s_nop 0
	global_load_lds_dwordx4 v[4:5], off
	s_mov_b32 m0, s0
	v_mov_b32_e32 v95, s15
	s_mov_b64 s[0:1], 0x4000
	v_lshl_add_u64 v[14:15], v[94:95], 0, s[0:1]
	v_lshrrev_b32_e32 v1, 2, v0
	v_readfirstlane_b32 s23, v14
	s_mov_b32 s2, m0
	s_mov_b32 m0, s23
	s_nop 0
	global_load_lds_dwordx4 v[6:7], off
	s_mov_b32 m0, s2
	s_mov_b64 s[2:3], 0x2000
	v_lshl_add_u64 v[14:15], v[94:95], 0, s[2:3]
	v_and_b32_e32 v8, 0x60, v1
	v_readfirstlane_b32 s20, v14
	s_mov_b32 s4, m0
	s_mov_b32 m0, s20
	s_nop 0
	global_load_lds_dwordx4 v[10:11], off
	s_mov_b32 m0, s4
	s_mov_b64 s[4:5], 0x6000
	v_lshl_add_u64 v[10:11], v[94:95], 0, s[4:5]
	v_mov_b32_e32 v11, s15
	v_readfirstlane_b32 s21, v10
	s_mov_b32 s6, m0
	s_mov_b32 m0, s21
	s_nop 0
	global_load_lds_dwordx4 v[12:13], off
	s_mov_b32 m0, s6
	v_add_u32_e32 v10, 0x8000, v94
	s_mov_b64 s[6:7], 0x80
	v_lshl_add_u64 v[12:13], v[4:5], 0, s[6:7]
	v_readfirstlane_b32 s16, v10
	s_mov_b32 s14, m0
	s_mov_b32 m0, s16
	s_nop 0
	global_load_lds_dwordx4 v[12:13], off
	s_mov_b32 m0, s14
	v_lshl_add_u64 v[14:15], v[10:11], 0, s[0:1]
	v_lshl_add_u64 v[12:13], v[6:7], 0, s[6:7]
	v_readfirstlane_b32 s18, v14
	s_mov_b32 s6, m0
	s_mov_b32 m0, s18
	s_nop 0
	global_load_lds_dwordx4 v[12:13], off
	s_mov_b32 m0, s6
	s_mov_b64 s[14:15], 0x22080
	v_lshl_add_u64 v[14:15], v[10:11], 0, s[2:3]
	v_lshl_add_u64 v[12:13], v[4:5], 0, s[14:15]
	v_readfirstlane_b32 s6, v14
	s_mov_b32 s7, m0
	s_mov_b32 m0, s6
	s_nop 0
	global_load_lds_dwordx4 v[12:13], off
	s_mov_b32 m0, s7
	v_lshl_add_u64 v[10:11], v[10:11], 0, s[4:5]
	s_add_i32 s26, 0, 0x10000
	v_or_b32_e32 v16, v8, v9
	v_lshl_add_u64 v[12:13], v[6:7], 0, s[14:15]
	v_readfirstlane_b32 s14, v10
	s_mov_b32 s7, m0
	s_mov_b32 m0, s14
	s_nop 0
	global_load_lds_dwordx4 v[12:13], off
	s_mov_b32 m0, s7
	v_add_u32_e32 v10, s26, v2
	v_mov_b32_e32 v11, v95
	s_mov_b64 s[24:25], 0x100
	v_lshlrev_b32_e32 v102, 7, v16
	v_lshl_add_u64 v[12:13], v[4:5], 0, s[24:25]
	v_readfirstlane_b32 s7, v10
	v_lshl_add_u64 v[10:11], v[10:11], 0, s[0:1]
	v_lshlrev_b32_e32 v103, 4, v17
	s_mov_b32 s15, m0
	s_mov_b32 m0, s7
	s_nop 0
	global_load_lds_dwordx4 v[12:13], off
	s_mov_b32 m0, s15
	v_lshl_add_u64 v[12:13], v[6:7], 0, s[24:25]
	v_add_u32_e32 v11, 0, v102
	v_add_u32_e32 v46, 0, v62
	v_add_u32_e32 v106, 0x10000, v94
	v_mov_b32_e32 v107, v95
	s_mov_b64 s[24:25], 0x22100
	v_readfirstlane_b32 s7, v10
	s_mov_b32 s15, m0
	s_mov_b32 m0, s7
	s_nop 0
	global_load_lds_dwordx4 v[12:13], off
	s_mov_b32 m0, s15
	v_add_u32_e32 v2, v11, v103
	v_add_u32_e32 v10, v46, v103
	v_lshlrev_b32_e32 v104, 4, v38
	v_lshl_add_u64 v[12:13], v[4:5], 0, s[24:25]
	v_lshl_add_u64 v[38:39], v[106:107], 0, s[2:3]
	s_waitcnt vmcnt(6)
	s_barrier
	ds_read_b128 v[14:17], v2
	ds_read_b128 v[18:21], v2 offset:2048
	ds_read_b128 v[22:25], v10 offset:16384
	ds_read_b128 v[26:29], v10 offset:18432
	ds_read_b128 v[30:33], v10 offset:20480
	ds_read_b128 v[34:37], v10 offset:22528
	v_readfirstlane_b32 s7, v38
	s_mov_b32 s15, m0
	s_mov_b32 m0, s7
	s_nop 0
	global_load_lds_dwordx4 v[12:13], off
	s_mov_b32 m0, s15
	v_lshl_add_u64 v[12:13], v[6:7], 0, s[24:25]
	v_lshl_add_u64 v[38:39], v[106:107], 0, s[4:5]
	v_or_b32_e32 v105, 0x4000, v62
	v_readfirstlane_b32 s15, v38
	s_mov_b32 s17, m0
	s_mov_b32 m0, s15
	s_nop 0
	global_load_lds_dwordx4 v[12:13], off
	s_mov_b32 m0, s17
	v_add_u32_e32 v12, v11, v104
	v_add_u32_e32 v11, v46, v104
	ds_read_b128 v[38:41], v12
	ds_read_b128 v[42:45], v12 offset:2048
	ds_read_b128 v[46:49], v11 offset:16384
	ds_read_b128 v[50:53], v11 offset:18432
	ds_read_b128 v[54:57], v11 offset:20480
	ds_read_b128 v[58:61], v11 offset:22528
	s_waitcnt lgkmcnt(9)
	v_mfma_f32_16x16x32_f16 v[62:65], v[14:17], v[22:25], 0
	s_waitcnt lgkmcnt(8)
	v_mfma_f32_16x16x32_f16 v[66:69], v[14:17], v[26:29], 0
	s_waitcnt lgkmcnt(7)
	v_mfma_f32_16x16x32_f16 v[70:73], v[14:17], v[30:33], 0
	s_waitcnt lgkmcnt(6)
	v_mfma_f32_16x16x32_f16 v[14:17], v[14:17], v[34:37], 0
	v_mfma_f32_16x16x32_f16 v[22:25], v[18:21], v[22:25], 0
	v_mfma_f32_16x16x32_f16 v[26:29], v[18:21], v[26:29], 0
	v_mfma_f32_16x16x32_f16 v[30:33], v[18:21], v[30:33], 0
	v_mfma_f32_16x16x32_f16 v[18:21], v[18:21], v[34:37], 0
	v_add_u32_e32 v94, 0x18000, v94
	s_mov_b64 s[24:25], 0x180
	s_waitcnt vmcnt(4)
	s_barrier
	v_lshl_add_u64 v[34:35], v[4:5], 0, s[24:25]
	v_readfirstlane_b32 s17, v94
	s_mov_b32 s19, m0
	s_mov_b32 m0, s17
	s_nop 0
	global_load_lds_dwordx4 v[34:35], off
	s_mov_b32 m0, s19
	v_lshl_add_u64 v[36:37], v[94:95], 0, s[0:1]
	v_lshl_add_u64 v[34:35], v[6:7], 0, s[24:25]
	v_readfirstlane_b32 s19, v36
	s_mov_b32 s24, m0
	s_mov_b32 m0, s19
	s_nop 0
	global_load_lds_dwordx4 v[34:35], off
	s_mov_b32 m0, s24
	ds_read_b128 v[34:37], v2 offset:32768
	ds_read_b128 v[74:77], v2 offset:34816
	ds_read_b128 v[78:81], v10 offset:49152
	ds_read_b128 v[82:85], v10 offset:51200
	ds_read_b128 v[86:89], v10 offset:53248
	ds_read_b128 v[90:93], v10 offset:55296
	s_waitcnt lgkmcnt(9)
	v_mfma_f32_16x16x32_f16 v[62:65], v[38:41], v[46:49], v[62:65]
	s_waitcnt lgkmcnt(8)
	v_mfma_f32_16x16x32_f16 v[66:69], v[38:41], v[50:53], v[66:69]
	s_waitcnt lgkmcnt(7)
	v_mfma_f32_16x16x32_f16 v[70:73], v[38:41], v[54:57], v[70:73]
	s_waitcnt lgkmcnt(6)
	v_mfma_f32_16x16x32_f16 v[14:17], v[38:41], v[58:61], v[14:17]
	v_mfma_f32_16x16x32_f16 v[22:25], v[42:45], v[46:49], v[22:25]
	v_mfma_f32_16x16x32_f16 v[26:29], v[42:45], v[50:53], v[26:29]
	v_mfma_f32_16x16x32_f16 v[30:33], v[42:45], v[54:57], v[30:33]
	v_mfma_f32_16x16x32_f16 v[18:21], v[42:45], v[58:61], v[18:21]
	s_mov_b64 s[24:25], 0x22180
	v_lshl_add_u64 v[40:41], v[94:95], 0, s[2:3]
	v_lshl_add_u64 v[38:39], v[4:5], 0, s[24:25]
	v_readfirstlane_b32 s2, v40
	s_mov_b32 s3, m0
	s_mov_b32 m0, s2
	s_nop 0
	global_load_lds_dwordx4 v[38:39], off
	s_mov_b32 m0, s3
	v_lshl_add_u64 v[40:41], v[94:95], 0, s[4:5]
	v_lshl_add_u64 v[38:39], v[6:7], 0, s[24:25]
	v_readfirstlane_b32 s3, v40
	s_mov_b32 s4, m0
	s_mov_b32 m0, s3
	s_nop 0
	global_load_lds_dwordx4 v[38:39], off
	s_mov_b32 m0, s4
	ds_read_b128 v[38:41], v12 offset:32768
	ds_read_b128 v[42:45], v12 offset:34816
	ds_read_b128 v[46:49], v11 offset:49152
	ds_read_b128 v[50:53], v11 offset:51200
	ds_read_b128 v[54:57], v11 offset:53248
	ds_read_b128 v[58:61], v11 offset:55296
	s_waitcnt lgkmcnt(9)
	v_mfma_f32_16x16x32_f16 v[62:65], v[34:37], v[78:81], v[62:65]
	s_waitcnt lgkmcnt(8)
	v_mfma_f32_16x16x32_f16 v[66:69], v[34:37], v[82:85], v[66:69]
	s_waitcnt lgkmcnt(7)
	v_mfma_f32_16x16x32_f16 v[70:73], v[34:37], v[86:89], v[70:73]
	s_waitcnt lgkmcnt(6)
	v_mfma_f32_16x16x32_f16 v[34:37], v[34:37], v[90:93], v[14:17]
	v_mfma_f32_16x16x32_f16 v[22:25], v[74:77], v[78:81], v[22:25]
	v_mfma_f32_16x16x32_f16 v[26:29], v[74:77], v[82:85], v[26:29]
	v_mfma_f32_16x16x32_f16 v[30:33], v[74:77], v[86:89], v[30:33]
	v_mfma_f32_16x16x32_f16 v[16:19], v[74:77], v[90:93], v[18:21]
	s_mov_b64 s[4:5], 0x200
	v_lshl_add_u64 v[14:15], v[4:5], 0, s[4:5]
	s_waitcnt vmcnt(4)
	s_barrier
	s_mov_b32 s24, m0
	s_mov_b32 m0, s22
	s_nop 0
	global_load_lds_dwordx4 v[14:15], off
	s_mov_b32 m0, s24
	v_lshl_add_u64 v[14:15], v[6:7], 0, s[4:5]
	s_mov_b32 s4, m0
	s_mov_b32 m0, s23
	s_nop 0
	global_load_lds_dwordx4 v[14:15], off
	s_mov_b32 m0, s4
	v_add_u32_e32 v15, s26, v102
	v_add_u32_e32 v14, v15, v103
	v_add3_u32 v13, s26, v103, v105
	ds_read_b128 v[74:77], v14
	ds_read_b128 v[78:81], v14 offset:2048
	ds_read_b128 v[82:85], v13
	ds_read_b128 v[86:89], v13 offset:2048
	ds_read_b128 v[90:93], v13 offset:4096
	ds_read_b128 v[94:97], v13 offset:6144
	s_waitcnt lgkmcnt(9)
	v_mfma_f32_16x16x32_f16 v[62:65], v[38:41], v[46:49], v[62:65]
	s_waitcnt lgkmcnt(8)
	v_mfma_f32_16x16x32_f16 v[66:69], v[38:41], v[50:53], v[66:69]
	s_waitcnt lgkmcnt(7)
	v_mfma_f32_16x16x32_f16 v[70:73], v[38:41], v[54:57], v[70:73]
	s_waitcnt lgkmcnt(6)
	v_mfma_f32_16x16x32_f16 v[34:37], v[38:41], v[58:61], v[34:37]
	v_mfma_f32_16x16x32_f16 v[20:23], v[42:45], v[46:49], v[22:25]
	v_mfma_f32_16x16x32_f16 v[24:27], v[42:45], v[50:53], v[26:29]
	v_mfma_f32_16x16x32_f16 v[28:31], v[42:45], v[54:57], v[30:33]
	v_mfma_f32_16x16x32_f16 v[38:41], v[42:45], v[58:61], v[16:19]
	s_mov_b64 s[4:5], 0x22200
	s_nop 1
	v_lshl_add_u64 v[16:17], v[4:5], 0, s[4:5]
	s_mov_b32 s24, m0
	s_mov_b32 m0, s20
	s_nop 0
	global_load_lds_dwordx4 v[16:17], off
	s_mov_b32 m0, s24
	v_lshl_add_u64 v[16:17], v[6:7], 0, s[4:5]
	s_mov_b32 s4, m0
	s_mov_b32 m0, s21
	s_nop 0
	global_load_lds_dwordx4 v[16:17], off
	s_mov_b32 m0, s4
	v_add_u32_e32 v16, v15, v104
	v_add3_u32 v15, s26, v104, v105
	ds_read_b128 v[42:45], v16
	ds_read_b128 v[46:49], v16 offset:2048
	ds_read_b128 v[50:53], v15
	ds_read_b128 v[54:57], v15 offset:2048
	ds_read_b128 v[58:61], v15 offset:4096
	ds_read_b128 v[98:101], v15 offset:6144
	s_waitcnt lgkmcnt(9)
	v_mfma_f32_16x16x32_f16 v[62:65], v[74:77], v[82:85], v[62:65]
	s_waitcnt lgkmcnt(8)
	v_mfma_f32_16x16x32_f16 v[66:69], v[74:77], v[86:89], v[66:69]
	s_waitcnt lgkmcnt(7)
	v_mfma_f32_16x16x32_f16 v[70:73], v[74:77], v[90:93], v[70:73]
	s_waitcnt lgkmcnt(6)
	v_mfma_f32_16x16x32_f16 v[32:35], v[74:77], v[94:97], v[34:37]
	v_mfma_f32_16x16x32_f16 v[20:23], v[78:81], v[82:85], v[20:23]
	v_mfma_f32_16x16x32_f16 v[24:27], v[78:81], v[86:89], v[24:27]
	v_mfma_f32_16x16x32_f16 v[28:31], v[78:81], v[90:93], v[28:31]
	v_mfma_f32_16x16x32_f16 v[36:39], v[78:81], v[94:97], v[38:41]
	s_mov_b64 s[4:5], 0x280
	s_waitcnt vmcnt(4)
	s_barrier
	v_lshl_add_u64 v[18:19], v[4:5], 0, s[4:5]
	s_mov_b32 s24, m0
	s_mov_b32 m0, s16
	s_nop 0
	global_load_lds_dwordx4 v[18:19], off
	s_mov_b32 m0, s24
	v_lshl_add_u64 v[18:19], v[6:7], 0, s[4:5]
	s_add_i32 s24, 0, 0x18000
	s_mov_b32 s4, m0
	s_mov_b32 m0, s18
	s_nop 0
	global_load_lds_dwordx4 v[18:19], off
	s_mov_b32 m0, s4
	v_add_u32_e32 v19, s24, v102
	v_add_u32_e32 v17, v19, v103
	v_add3_u32 v18, s24, v103, v105
	ds_read_b128 v[74:77], v17
	ds_read_b128 v[78:81], v17 offset:2048
	ds_read_b128 v[82:85], v18
	ds_read_b128 v[86:89], v18 offset:2048
	ds_read_b128 v[90:93], v18 offset:4096
	ds_read_b128 v[94:97], v18 offset:6144
	s_waitcnt lgkmcnt(9)
	v_mfma_f32_16x16x32_f16 v[62:65], v[42:45], v[50:53], v[62:65]
	s_waitcnt lgkmcnt(8)
	v_mfma_f32_16x16x32_f16 v[66:69], v[42:45], v[54:57], v[66:69]
	s_waitcnt lgkmcnt(7)
	v_mfma_f32_16x16x32_f16 v[70:73], v[42:45], v[58:61], v[70:73]
	s_waitcnt lgkmcnt(6)
	v_mfma_f32_16x16x32_f16 v[32:35], v[42:45], v[98:101], v[32:35]
	v_mfma_f32_16x16x32_f16 v[40:43], v[46:49], v[50:53], v[20:23]
	v_mfma_f32_16x16x32_f16 v[22:25], v[46:49], v[54:57], v[24:27]
	v_mfma_f32_16x16x32_f16 v[26:29], v[46:49], v[58:61], v[28:31]
	v_mfma_f32_16x16x32_f16 v[36:39], v[46:49], v[98:101], v[36:39]
	s_mov_b64 s[4:5], 0x22280
	v_lshl_add_u64 v[20:21], v[4:5], 0, s[4:5]
	s_mov_b32 s25, m0
	s_mov_b32 m0, s6
	s_nop 0
	global_load_lds_dwordx4 v[20:21], off
	s_mov_b32 m0, s25
	v_lshl_add_u64 v[20:21], v[6:7], 0, s[4:5]
	s_mov_b32 s4, m0
	s_mov_b32 m0, s14
	s_nop 0
	global_load_lds_dwordx4 v[20:21], off
	s_mov_b32 m0, s4
	v_add_u32_e32 v19, v19, v104
	v_add3_u32 v20, s24, v104, v105
	ds_read_b128 v[44:47], v19
	ds_read_b128 v[48:51], v19 offset:2048
	ds_read_b128 v[52:55], v20
	ds_read_b128 v[56:59], v20 offset:2048
	ds_read_b128 v[98:101], v20 offset:4096
	ds_read_b128 v[102:105], v20 offset:6144
	s_waitcnt lgkmcnt(9)
	v_mfma_f32_16x16x32_f16 v[60:63], v[74:77], v[82:85], v[62:65]
	s_waitcnt lgkmcnt(8)
	v_mfma_f32_16x16x32_f16 v[64:67], v[74:77], v[86:89], v[66:69]
	s_waitcnt lgkmcnt(7)
	v_mfma_f32_16x16x32_f16 v[68:71], v[74:77], v[90:93], v[70:73]
	s_waitcnt lgkmcnt(6)
	v_mfma_f32_16x16x32_f16 v[30:33], v[74:77], v[94:97], v[32:35]
	v_mfma_f32_16x16x32_f16 v[40:43], v[78:81], v[82:85], v[40:43]
	v_mfma_f32_16x16x32_f16 v[22:25], v[78:81], v[86:89], v[22:25]
	v_mfma_f32_16x16x32_f16 v[26:29], v[78:81], v[90:93], v[26:29]
	v_mfma_f32_16x16x32_f16 v[34:37], v[78:81], v[94:97], v[36:39]
	s_mov_b64 s[24:25], 0x300
	s_waitcnt vmcnt(4)
	s_barrier
	s_nop 0
	v_lshl_add_u64 v[38:39], v[4:5], 0, s[24:25]
	v_readfirstlane_b32 s4, v106
	s_mov_b32 s5, m0
	s_mov_b32 m0, s4
	s_nop 0
	global_load_lds_dwordx4 v[38:39], off
	s_mov_b32 m0, s5
	v_lshl_add_u64 v[72:73], v[106:107], 0, s[0:1]
	v_lshl_add_u64 v[38:39], v[6:7], 0, s[24:25]
	v_readfirstlane_b32 s0, v72
	s_mov_b32 s1, m0
	s_mov_b32 m0, s0
	s_nop 0
	global_load_lds_dwordx4 v[38:39], off
	s_mov_b32 m0, s1
	ds_read_b128 v[72:75], v2
	ds_read_b128 v[76:79], v2 offset:2048
	ds_read_b128 v[80:83], v10 offset:16384
	ds_read_b128 v[84:87], v10 offset:18432
	ds_read_b128 v[88:91], v10 offset:20480
	ds_read_b128 v[92:95], v10 offset:22528
	s_waitcnt lgkmcnt(9)
	v_mfma_f32_16x16x32_f16 v[60:63], v[44:47], v[52:55], v[60:63]
	s_waitcnt lgkmcnt(8)
	v_mfma_f32_16x16x32_f16 v[64:67], v[44:47], v[56:59], v[64:67]
	s_waitcnt lgkmcnt(7)
	v_mfma_f32_16x16x32_f16 v[68:71], v[44:47], v[98:101], v[68:71]
	s_waitcnt lgkmcnt(6)
	v_mfma_f32_16x16x32_f16 v[30:33], v[44:47], v[102:105], v[30:33]
	v_mfma_f32_16x16x32_f16 v[38:41], v[48:51], v[52:55], v[40:43]
	v_mfma_f32_16x16x32_f16 v[22:25], v[48:51], v[56:59], v[22:25]
	v_mfma_f32_16x16x32_f16 v[26:29], v[48:51], v[98:101], v[26:29]
	v_mfma_f32_16x16x32_f16 v[34:37], v[48:51], v[102:105], v[34:37]
	s_mov_b64 s[24:25], 0x22300
	v_lshl_add_u64 v[42:43], v[4:5], 0, s[24:25]
	s_mov_b32 s1, m0
	s_mov_b32 m0, s7
	s_nop 0
	global_load_lds_dwordx4 v[42:43], off
	s_mov_b32 m0, s1
	v_lshl_add_u64 v[42:43], v[6:7], 0, s[24:25]
	s_mov_b32 s1, m0
	s_mov_b32 m0, s15
	s_nop 0
	global_load_lds_dwordx4 v[42:43], off
	s_mov_b32 m0, s1
	ds_read_b128 v[42:45], v12
	ds_read_b128 v[46:49], v12 offset:2048
	ds_read_b128 v[50:53], v11 offset:16384
	ds_read_b128 v[54:57], v11 offset:18432
	ds_read_b128 v[96:99], v11 offset:20480
	ds_read_b128 v[100:103], v11 offset:22528
	s_waitcnt lgkmcnt(9)
	v_mfma_f32_16x16x32_f16 v[58:61], v[72:75], v[80:83], v[60:63]
	s_waitcnt lgkmcnt(8)
	v_mfma_f32_16x16x32_f16 v[62:65], v[72:75], v[84:87], v[64:67]
	s_waitcnt lgkmcnt(7)
	v_mfma_f32_16x16x32_f16 v[66:69], v[72:75], v[88:91], v[68:71]
	s_waitcnt lgkmcnt(6)
	v_mfma_f32_16x16x32_f16 v[30:33], v[72:75], v[92:95], v[30:33]
	v_mfma_f32_16x16x32_f16 v[38:41], v[76:79], v[80:83], v[38:41]
	v_mfma_f32_16x16x32_f16 v[22:25], v[76:79], v[84:87], v[22:25]
	v_mfma_f32_16x16x32_f16 v[26:29], v[76:79], v[88:91], v[26:29]
	v_mfma_f32_16x16x32_f16 v[34:37], v[76:79], v[92:95], v[34:37]
	s_mov_b64 s[24:25], 0x380
	s_waitcnt vmcnt(4)
	s_barrier
	v_lshl_add_u64 v[70:71], v[4:5], 0, s[24:25]
	s_mov_b32 s1, m0
	s_mov_b32 m0, s17
	s_nop 0
	global_load_lds_dwordx4 v[70:71], off
	s_mov_b32 m0, s1
	v_lshl_add_u64 v[70:71], v[6:7], 0, s[24:25]
	s_mov_b32 s1, m0
	s_mov_b32 m0, s19
	s_nop 0
	global_load_lds_dwordx4 v[70:71], off
	s_mov_b32 m0, s1
	ds_read_b128 v[70:73], v2 offset:32768
	ds_read_b128 v[74:77], v2 offset:34816
	ds_read_b128 v[78:81], v10 offset:49152
	ds_read_b128 v[82:85], v10 offset:51200
	ds_read_b128 v[86:89], v10 offset:53248
	ds_read_b128 v[90:93], v10 offset:55296
	s_waitcnt lgkmcnt(9)
	v_mfma_f32_16x16x32_f16 v[58:61], v[42:45], v[50:53], v[58:61]
	s_waitcnt lgkmcnt(8)
	v_mfma_f32_16x16x32_f16 v[62:65], v[42:45], v[54:57], v[62:65]
	s_waitcnt lgkmcnt(7)
	v_mfma_f32_16x16x32_f16 v[66:69], v[42:45], v[96:99], v[66:69]
	s_waitcnt lgkmcnt(6)
	v_mfma_f32_16x16x32_f16 v[30:33], v[42:45], v[100:103], v[30:33]
	v_mfma_f32_16x16x32_f16 v[38:41], v[46:49], v[50:53], v[38:41]
	v_mfma_f32_16x16x32_f16 v[22:25], v[46:49], v[54:57], v[22:25]
	v_mfma_f32_16x16x32_f16 v[26:29], v[46:49], v[96:99], v[26:29]
	v_mfma_f32_16x16x32_f16 v[34:37], v[46:49], v[100:103], v[34:37]
	s_mov_b64 s[24:25], 0x22380
	v_lshl_add_u64 v[42:43], v[4:5], 0, s[24:25]
	s_mov_b32 s1, m0
	s_mov_b32 m0, s2
	s_nop 0
	global_load_lds_dwordx4 v[42:43], off
	s_mov_b32 m0, s1
	v_lshl_add_u64 v[42:43], v[6:7], 0, s[24:25]
	s_mov_b32 s1, m0
	s_mov_b32 m0, s3
	s_nop 0
	global_load_lds_dwordx4 v[42:43], off
	s_mov_b32 m0, s1
	ds_read_b128 v[42:45], v12 offset:32768
	ds_read_b128 v[46:49], v12 offset:34816
	ds_read_b128 v[50:53], v11 offset:49152
	ds_read_b128 v[54:57], v11 offset:51200
	ds_read_b128 v[94:97], v11 offset:53248
	ds_read_b128 v[98:101], v11 offset:55296
	s_waitcnt lgkmcnt(9)
	v_mfma_f32_16x16x32_f16 v[58:61], v[70:73], v[78:81], v[58:61]
	s_waitcnt lgkmcnt(8)
	v_mfma_f32_16x16x32_f16 v[62:65], v[70:73], v[82:85], v[62:65]
	s_waitcnt lgkmcnt(7)
	v_mfma_f32_16x16x32_f16 v[66:69], v[70:73], v[86:89], v[66:69]
	s_waitcnt lgkmcnt(6)
	v_mfma_f32_16x16x32_f16 v[30:33], v[70:73], v[90:93], v[30:33]
	v_mfma_f32_16x16x32_f16 v[38:41], v[74:77], v[78:81], v[38:41]
	v_mfma_f32_16x16x32_f16 v[22:25], v[74:77], v[82:85], v[22:25]
	v_mfma_f32_16x16x32_f16 v[26:29], v[74:77], v[86:89], v[26:29]
	v_mfma_f32_16x16x32_f16 v[34:37], v[74:77], v[90:93], v[34:37]
	s_mov_b64 s[24:25], 0x400
	s_waitcnt vmcnt(4)
	s_barrier
	v_lshl_add_u64 v[70:71], v[4:5], 0, s[24:25]
	s_mov_b32 s1, m0
	s_mov_b32 m0, s22
	s_nop 0
	global_load_lds_dwordx4 v[70:71], off
	s_mov_b32 m0, s1
	v_lshl_add_u64 v[70:71], v[6:7], 0, s[24:25]
	s_mov_b32 s1, m0
	s_mov_b32 m0, s23
	s_nop 0
	global_load_lds_dwordx4 v[70:71], off
	s_mov_b32 m0, s1
	ds_read_b128 v[70:73], v14
	ds_read_b128 v[74:77], v14 offset:2048
	ds_read_b128 v[78:81], v13
	ds_read_b128 v[82:85], v13 offset:2048
	ds_read_b128 v[86:89], v13 offset:4096
	ds_read_b128 v[90:93], v13 offset:6144
	s_waitcnt lgkmcnt(9)
	v_mfma_f32_16x16x32_f16 v[58:61], v[42:45], v[50:53], v[58:61]
	s_waitcnt lgkmcnt(8)
	v_mfma_f32_16x16x32_f16 v[62:65], v[42:45], v[54:57], v[62:65]
	s_waitcnt lgkmcnt(7)
	v_mfma_f32_16x16x32_f16 v[66:69], v[42:45], v[94:97], v[66:69]
	s_waitcnt lgkmcnt(6)
	v_mfma_f32_16x16x32_f16 v[30:33], v[42:45], v[98:101], v[30:33]
	v_mfma_f32_16x16x32_f16 v[38:41], v[46:49], v[50:53], v[38:41]
	v_mfma_f32_16x16x32_f16 v[22:25], v[46:49], v[54:57], v[22:25]
	v_mfma_f32_16x16x32_f16 v[26:29], v[46:49], v[94:97], v[26:29]
	v_mfma_f32_16x16x32_f16 v[34:37], v[46:49], v[98:101], v[34:37]
	s_mov_b64 s[24:25], 0x22400
	v_lshl_add_u64 v[42:43], v[4:5], 0, s[24:25]
	s_mov_b32 s1, m0
	s_mov_b32 m0, s20
	s_nop 0
	global_load_lds_dwordx4 v[42:43], off
	s_mov_b32 m0, s1
	v_lshl_add_u64 v[42:43], v[6:7], 0, s[24:25]
	s_mov_b32 s1, m0
	s_mov_b32 m0, s21
	s_nop 0
	global_load_lds_dwordx4 v[42:43], off
	s_mov_b32 m0, s1
	ds_read_b128 v[42:45], v16
	ds_read_b128 v[46:49], v16 offset:2048
	ds_read_b128 v[50:53], v15
	ds_read_b128 v[54:57], v15 offset:2048
	ds_read_b128 v[94:97], v15 offset:4096
	ds_read_b128 v[98:101], v15 offset:6144
	s_waitcnt lgkmcnt(9)
	v_mfma_f32_16x16x32_f16 v[58:61], v[70:73], v[78:81], v[58:61]
	s_waitcnt lgkmcnt(8)
	v_mfma_f32_16x16x32_f16 v[62:65], v[70:73], v[82:85], v[62:65]
	s_waitcnt lgkmcnt(7)
	v_mfma_f32_16x16x32_f16 v[66:69], v[70:73], v[86:89], v[66:69]
	s_waitcnt lgkmcnt(6)
	v_mfma_f32_16x16x32_f16 v[30:33], v[70:73], v[90:93], v[30:33]
	v_mfma_f32_16x16x32_f16 v[38:41], v[74:77], v[78:81], v[38:41]
	v_mfma_f32_16x16x32_f16 v[22:25], v[74:77], v[82:85], v[22:25]
	v_mfma_f32_16x16x32_f16 v[26:29], v[74:77], v[86:89], v[26:29]
	v_mfma_f32_16x16x32_f16 v[34:37], v[74:77], v[90:93], v[34:37]
	s_mov_b64 s[24:25], 0x480
	s_waitcnt vmcnt(4)
	s_barrier
	v_lshl_add_u64 v[70:71], v[4:5], 0, s[24:25]
	s_mov_b32 s1, m0
	s_mov_b32 m0, s16
	s_nop 0
	global_load_lds_dwordx4 v[70:71], off
	s_mov_b32 m0, s1
	v_lshl_add_u64 v[70:71], v[6:7], 0, s[24:25]
	s_mov_b32 s1, m0
	s_mov_b32 m0, s18
	s_nop 0
	global_load_lds_dwordx4 v[70:71], off
	s_mov_b32 m0, s1
	ds_read_b128 v[70:73], v17
	ds_read_b128 v[74:77], v17 offset:2048
	ds_read_b128 v[78:81], v18
	ds_read_b128 v[82:85], v18 offset:2048
	ds_read_b128 v[86:89], v18 offset:4096
	ds_read_b128 v[90:93], v18 offset:6144
	s_waitcnt lgkmcnt(9)
	v_mfma_f32_16x16x32_f16 v[58:61], v[42:45], v[50:53], v[58:61]
	s_waitcnt lgkmcnt(8)
	v_mfma_f32_16x16x32_f16 v[62:65], v[42:45], v[54:57], v[62:65]
	s_waitcnt lgkmcnt(7)
	v_mfma_f32_16x16x32_f16 v[66:69], v[42:45], v[94:97], v[66:69]
	s_waitcnt lgkmcnt(6)
	v_mfma_f32_16x16x32_f16 v[30:33], v[42:45], v[98:101], v[30:33]
	v_mfma_f32_16x16x32_f16 v[38:41], v[46:49], v[50:53], v[38:41]
	v_mfma_f32_16x16x32_f16 v[22:25], v[46:49], v[54:57], v[22:25]
	v_mfma_f32_16x16x32_f16 v[26:29], v[46:49], v[94:97], v[26:29]
	v_mfma_f32_16x16x32_f16 v[34:37], v[46:49], v[98:101], v[34:37]
	s_mov_b64 s[24:25], 0x22480
	v_lshl_add_u64 v[42:43], v[4:5], 0, s[24:25]
	s_mov_b32 s1, m0
	s_mov_b32 m0, s6
	s_nop 0
	global_load_lds_dwordx4 v[42:43], off
	s_mov_b32 m0, s1
	v_lshl_add_u64 v[42:43], v[6:7], 0, s[24:25]
	s_mov_b32 s1, m0
	s_mov_b32 m0, s14
	s_nop 0
	global_load_lds_dwordx4 v[42:43], off
	s_mov_b32 m0, s1
	ds_read_b128 v[42:45], v19
	ds_read_b128 v[46:49], v19 offset:2048
	ds_read_b128 v[50:53], v20
	ds_read_b128 v[54:57], v20 offset:2048
	ds_read_b128 v[94:97], v20 offset:4096
	ds_read_b128 v[98:101], v20 offset:6144
	s_waitcnt lgkmcnt(9)
	v_mfma_f32_16x16x32_f16 v[58:61], v[70:73], v[78:81], v[58:61]
	s_waitcnt lgkmcnt(8)
	v_mfma_f32_16x16x32_f16 v[62:65], v[70:73], v[82:85], v[62:65]
	s_waitcnt lgkmcnt(7)
	v_mfma_f32_16x16x32_f16 v[66:69], v[70:73], v[86:89], v[66:69]
	s_waitcnt lgkmcnt(6)
	v_mfma_f32_16x16x32_f16 v[30:33], v[70:73], v[90:93], v[30:33]
	v_mfma_f32_16x16x32_f16 v[38:41], v[74:77], v[78:81], v[38:41]
	v_mfma_f32_16x16x32_f16 v[22:25], v[74:77], v[82:85], v[22:25]
	v_mfma_f32_16x16x32_f16 v[26:29], v[74:77], v[86:89], v[26:29]
	v_mfma_f32_16x16x32_f16 v[34:37], v[74:77], v[90:93], v[34:37]
	s_mov_b64 s[24:25], 0x500
	s_waitcnt vmcnt(4)
	s_barrier
	v_lshl_add_u64 v[70:71], v[4:5], 0, s[24:25]
	s_mov_b32 s1, m0
	s_mov_b32 m0, s4
	s_nop 0
	global_load_lds_dwordx4 v[70:71], off
	s_mov_b32 m0, s1
	v_lshl_add_u64 v[70:71], v[6:7], 0, s[24:25]
	s_mov_b32 s1, m0
	s_mov_b32 m0, s0
	s_nop 0
	global_load_lds_dwordx4 v[70:71], off
	s_mov_b32 m0, s1
	ds_read_b128 v[70:73], v2
	ds_read_b128 v[74:77], v2 offset:2048
	ds_read_b128 v[78:81], v10 offset:16384
	ds_read_b128 v[82:85], v10 offset:18432
	ds_read_b128 v[86:89], v10 offset:20480
	ds_read_b128 v[90:93], v10 offset:22528
	s_waitcnt lgkmcnt(9)
	v_mfma_f32_16x16x32_f16 v[58:61], v[42:45], v[50:53], v[58:61]
	s_waitcnt lgkmcnt(8)
	v_mfma_f32_16x16x32_f16 v[62:65], v[42:45], v[54:57], v[62:65]
	s_waitcnt lgkmcnt(7)
	v_mfma_f32_16x16x32_f16 v[66:69], v[42:45], v[94:97], v[66:69]
	s_waitcnt lgkmcnt(6)
	v_mfma_f32_16x16x32_f16 v[30:33], v[42:45], v[98:101], v[30:33]
	v_mfma_f32_16x16x32_f16 v[38:41], v[46:49], v[50:53], v[38:41]
	v_mfma_f32_16x16x32_f16 v[22:25], v[46:49], v[54:57], v[22:25]
	v_mfma_f32_16x16x32_f16 v[26:29], v[46:49], v[94:97], v[26:29]
	v_mfma_f32_16x16x32_f16 v[34:37], v[46:49], v[98:101], v[34:37]
	s_mov_b64 s[24:25], 0x22500
	v_lshl_add_u64 v[42:43], v[4:5], 0, s[24:25]
	s_mov_b32 s1, m0
	s_mov_b32 m0, s7
	s_nop 0
	global_load_lds_dwordx4 v[42:43], off
	s_mov_b32 m0, s1
	v_lshl_add_u64 v[42:43], v[6:7], 0, s[24:25]
	s_mov_b32 s1, m0
	s_mov_b32 m0, s15
	s_nop 0
	global_load_lds_dwordx4 v[42:43], off
	s_mov_b32 m0, s1
	ds_read_b128 v[42:45], v12
	ds_read_b128 v[46:49], v12 offset:2048
	ds_read_b128 v[50:53], v11 offset:16384
	ds_read_b128 v[54:57], v11 offset:18432
	ds_read_b128 v[94:97], v11 offset:20480
	ds_read_b128 v[98:101], v11 offset:22528
	s_waitcnt lgkmcnt(9)
	v_mfma_f32_16x16x32_f16 v[58:61], v[70:73], v[78:81], v[58:61]
	s_waitcnt lgkmcnt(8)
	v_mfma_f32_16x16x32_f16 v[62:65], v[70:73], v[82:85], v[62:65]
	s_waitcnt lgkmcnt(7)
	v_mfma_f32_16x16x32_f16 v[66:69], v[70:73], v[86:89], v[66:69]
	s_waitcnt lgkmcnt(6)
	v_mfma_f32_16x16x32_f16 v[30:33], v[70:73], v[90:93], v[30:33]
	v_mfma_f32_16x16x32_f16 v[38:41], v[74:77], v[78:81], v[38:41]
	v_mfma_f32_16x16x32_f16 v[22:25], v[74:77], v[82:85], v[22:25]
	v_mfma_f32_16x16x32_f16 v[26:29], v[74:77], v[86:89], v[26:29]
	v_mfma_f32_16x16x32_f16 v[34:37], v[74:77], v[90:93], v[34:37]
	s_mov_b64 s[24:25], 0x580
	s_waitcnt vmcnt(4)
	s_barrier
	v_lshl_add_u64 v[70:71], v[4:5], 0, s[24:25]
	s_mov_b32 s1, m0
	s_mov_b32 m0, s17
	s_nop 0
	global_load_lds_dwordx4 v[70:71], off
	s_mov_b32 m0, s1
	v_lshl_add_u64 v[70:71], v[6:7], 0, s[24:25]
	s_mov_b32 s1, m0
	s_mov_b32 m0, s19
	s_nop 0
	global_load_lds_dwordx4 v[70:71], off
	s_mov_b32 m0, s1
	ds_read_b128 v[70:73], v2 offset:32768
	ds_read_b128 v[74:77], v2 offset:34816
	ds_read_b128 v[78:81], v10 offset:49152
	ds_read_b128 v[82:85], v10 offset:51200
	ds_read_b128 v[86:89], v10 offset:53248
	ds_read_b128 v[90:93], v10 offset:55296
	s_waitcnt lgkmcnt(9)
	v_mfma_f32_16x16x32_f16 v[58:61], v[42:45], v[50:53], v[58:61]
	s_waitcnt lgkmcnt(8)
	v_mfma_f32_16x16x32_f16 v[62:65], v[42:45], v[54:57], v[62:65]
	s_waitcnt lgkmcnt(7)
	v_mfma_f32_16x16x32_f16 v[66:69], v[42:45], v[94:97], v[66:69]
	s_waitcnt lgkmcnt(6)
	v_mfma_f32_16x16x32_f16 v[30:33], v[42:45], v[98:101], v[30:33]
	v_mfma_f32_16x16x32_f16 v[38:41], v[46:49], v[50:53], v[38:41]
	v_mfma_f32_16x16x32_f16 v[22:25], v[46:49], v[54:57], v[22:25]
	v_mfma_f32_16x16x32_f16 v[26:29], v[46:49], v[94:97], v[26:29]
	v_mfma_f32_16x16x32_f16 v[34:37], v[46:49], v[98:101], v[34:37]
	s_mov_b64 s[24:25], 0x22580
	v_lshl_add_u64 v[42:43], v[4:5], 0, s[24:25]
	s_mov_b32 s1, m0
	s_mov_b32 m0, s2
	s_nop 0
	global_load_lds_dwordx4 v[42:43], off
	s_mov_b32 m0, s1
	v_lshl_add_u64 v[42:43], v[6:7], 0, s[24:25]
	s_mov_b32 s1, m0
	s_mov_b32 m0, s3
	s_nop 0
	global_load_lds_dwordx4 v[42:43], off
	s_mov_b32 m0, s1
	ds_read_b128 v[42:45], v12 offset:32768
	ds_read_b128 v[46:49], v12 offset:34816
	ds_read_b128 v[50:53], v11 offset:49152
	ds_read_b128 v[54:57], v11 offset:51200
	ds_read_b128 v[94:97], v11 offset:53248
	ds_read_b128 v[98:101], v11 offset:55296
	s_waitcnt lgkmcnt(9)
	v_mfma_f32_16x16x32_f16 v[58:61], v[70:73], v[78:81], v[58:61]
	s_waitcnt lgkmcnt(8)
	v_mfma_f32_16x16x32_f16 v[62:65], v[70:73], v[82:85], v[62:65]
	s_waitcnt lgkmcnt(7)
	v_mfma_f32_16x16x32_f16 v[66:69], v[70:73], v[86:89], v[66:69]
	s_waitcnt lgkmcnt(6)
	v_mfma_f32_16x16x32_f16 v[30:33], v[70:73], v[90:93], v[30:33]
	v_mfma_f32_16x16x32_f16 v[38:41], v[74:77], v[78:81], v[38:41]
	v_mfma_f32_16x16x32_f16 v[22:25], v[74:77], v[82:85], v[22:25]
	v_mfma_f32_16x16x32_f16 v[26:29], v[74:77], v[86:89], v[26:29]
	v_mfma_f32_16x16x32_f16 v[34:37], v[74:77], v[90:93], v[34:37]
	s_mov_b64 s[24:25], 0x600
	s_waitcnt vmcnt(4)
	s_barrier
	v_lshl_add_u64 v[70:71], v[4:5], 0, s[24:25]
	s_mov_b32 s1, m0
	s_mov_b32 m0, s22
	s_nop 0
	global_load_lds_dwordx4 v[70:71], off
	s_mov_b32 m0, s1
	v_lshl_add_u64 v[70:71], v[6:7], 0, s[24:25]
	s_mov_b32 s1, m0
	s_mov_b32 m0, s23
	s_nop 0
	global_load_lds_dwordx4 v[70:71], off
	s_mov_b32 m0, s1
	ds_read_b128 v[70:73], v14
	ds_read_b128 v[74:77], v14 offset:2048
	ds_read_b128 v[78:81], v13
	ds_read_b128 v[82:85], v13 offset:2048
	ds_read_b128 v[86:89], v13 offset:4096
	ds_read_b128 v[90:93], v13 offset:6144
	s_waitcnt lgkmcnt(9)
	v_mfma_f32_16x16x32_f16 v[58:61], v[42:45], v[50:53], v[58:61]
	s_waitcnt lgkmcnt(8)
	v_mfma_f32_16x16x32_f16 v[62:65], v[42:45], v[54:57], v[62:65]
	s_waitcnt lgkmcnt(7)
	v_mfma_f32_16x16x32_f16 v[66:69], v[42:45], v[94:97], v[66:69]
	s_waitcnt lgkmcnt(6)
	v_mfma_f32_16x16x32_f16 v[30:33], v[42:45], v[98:101], v[30:33]
	v_mfma_f32_16x16x32_f16 v[38:41], v[46:49], v[50:53], v[38:41]
	v_mfma_f32_16x16x32_f16 v[22:25], v[46:49], v[54:57], v[22:25]
	v_mfma_f32_16x16x32_f16 v[26:29], v[46:49], v[94:97], v[26:29]
	v_mfma_f32_16x16x32_f16 v[34:37], v[46:49], v[98:101], v[34:37]
	s_mov_b64 s[22:23], 0x22600
	v_lshl_add_u64 v[42:43], v[4:5], 0, s[22:23]
	s_mov_b32 s1, m0
	s_mov_b32 m0, s20
	s_nop 0
	global_load_lds_dwordx4 v[42:43], off
	s_mov_b32 m0, s1
	v_lshl_add_u64 v[42:43], v[6:7], 0, s[22:23]
	s_mov_b32 s1, m0
	s_mov_b32 m0, s21
	s_nop 0
	global_load_lds_dwordx4 v[42:43], off
	s_mov_b32 m0, s1
	ds_read_b128 v[42:45], v16
	ds_read_b128 v[46:49], v16 offset:2048
	ds_read_b128 v[50:53], v15
	ds_read_b128 v[54:57], v15 offset:2048
	ds_read_b128 v[94:97], v15 offset:4096
	ds_read_b128 v[98:101], v15 offset:6144
	s_waitcnt lgkmcnt(9)
	v_mfma_f32_16x16x32_f16 v[58:61], v[70:73], v[78:81], v[58:61]
	s_waitcnt lgkmcnt(8)
	v_mfma_f32_16x16x32_f16 v[62:65], v[70:73], v[82:85], v[62:65]
	s_waitcnt lgkmcnt(7)
	v_mfma_f32_16x16x32_f16 v[66:69], v[70:73], v[86:89], v[66:69]
	s_waitcnt lgkmcnt(6)
	v_mfma_f32_16x16x32_f16 v[30:33], v[70:73], v[90:93], v[30:33]
	v_mfma_f32_16x16x32_f16 v[38:41], v[74:77], v[78:81], v[38:41]
	v_mfma_f32_16x16x32_f16 v[22:25], v[74:77], v[82:85], v[22:25]
	v_mfma_f32_16x16x32_f16 v[26:29], v[74:77], v[86:89], v[26:29]
	v_mfma_f32_16x16x32_f16 v[34:37], v[74:77], v[90:93], v[34:37]
	s_mov_b64 s[20:21], 0x680
	s_waitcnt vmcnt(4)
	s_barrier
	v_lshl_add_u64 v[70:71], v[4:5], 0, s[20:21]
	s_mov_b32 s1, m0
	s_mov_b32 m0, s16
	s_nop 0
	global_load_lds_dwordx4 v[70:71], off
	s_mov_b32 m0, s1
	v_lshl_add_u64 v[70:71], v[6:7], 0, s[20:21]
	s_mov_b32 s1, m0
	s_mov_b32 m0, s18
	s_nop 0
	global_load_lds_dwordx4 v[70:71], off
	s_mov_b32 m0, s1
	ds_read_b128 v[70:73], v17
	ds_read_b128 v[74:77], v17 offset:2048
	ds_read_b128 v[78:81], v18
	ds_read_b128 v[82:85], v18 offset:2048
	ds_read_b128 v[86:89], v18 offset:4096
	ds_read_b128 v[90:93], v18 offset:6144
	s_waitcnt lgkmcnt(9)
	v_mfma_f32_16x16x32_f16 v[58:61], v[42:45], v[50:53], v[58:61]
	s_waitcnt lgkmcnt(8)
	v_mfma_f32_16x16x32_f16 v[62:65], v[42:45], v[54:57], v[62:65]
	s_waitcnt lgkmcnt(7)
	v_mfma_f32_16x16x32_f16 v[66:69], v[42:45], v[94:97], v[66:69]
	s_waitcnt lgkmcnt(6)
	v_mfma_f32_16x16x32_f16 v[30:33], v[42:45], v[98:101], v[30:33]
	v_mfma_f32_16x16x32_f16 v[38:41], v[46:49], v[50:53], v[38:41]
	v_mfma_f32_16x16x32_f16 v[22:25], v[46:49], v[54:57], v[22:25]
	v_mfma_f32_16x16x32_f16 v[26:29], v[46:49], v[94:97], v[26:29]
	v_mfma_f32_16x16x32_f16 v[34:37], v[46:49], v[98:101], v[34:37]
	s_mov_b64 s[20:21], 0x22680
	v_lshl_add_u64 v[42:43], v[4:5], 0, s[20:21]
	s_mov_b32 s1, m0
	s_mov_b32 m0, s6
	s_nop 0
	global_load_lds_dwordx4 v[42:43], off
	s_mov_b32 m0, s1
	v_lshl_add_u64 v[42:43], v[6:7], 0, s[20:21]
	s_mov_b32 s1, m0
	s_mov_b32 m0, s14
	s_nop 0
	global_load_lds_dwordx4 v[42:43], off
	s_mov_b32 m0, s1
	ds_read_b128 v[42:45], v19
	ds_read_b128 v[46:49], v19 offset:2048
	ds_read_b128 v[50:53], v20
	ds_read_b128 v[54:57], v20 offset:2048
	ds_read_b128 v[94:97], v20 offset:4096
	ds_read_b128 v[98:101], v20 offset:6144
	s_waitcnt lgkmcnt(9)
	v_mfma_f32_16x16x32_f16 v[58:61], v[70:73], v[78:81], v[58:61]
	s_waitcnt lgkmcnt(8)
	v_mfma_f32_16x16x32_f16 v[62:65], v[70:73], v[82:85], v[62:65]
	s_waitcnt lgkmcnt(7)
	v_mfma_f32_16x16x32_f16 v[66:69], v[70:73], v[86:89], v[66:69]
	s_waitcnt lgkmcnt(6)
	v_mfma_f32_16x16x32_f16 v[30:33], v[70:73], v[90:93], v[30:33]
	v_mfma_f32_16x16x32_f16 v[38:41], v[74:77], v[78:81], v[38:41]
	v_mfma_f32_16x16x32_f16 v[22:25], v[74:77], v[82:85], v[22:25]
	v_mfma_f32_16x16x32_f16 v[26:29], v[74:77], v[86:89], v[26:29]
	v_mfma_f32_16x16x32_f16 v[34:37], v[74:77], v[90:93], v[34:37]
	s_mov_b64 s[20:21], 0x700
	s_waitcnt vmcnt(4)
	s_barrier
	v_lshl_add_u64 v[70:71], v[4:5], 0, s[20:21]
	s_mov_b32 s1, m0
	s_mov_b32 m0, s4
	s_nop 0
	global_load_lds_dwordx4 v[70:71], off
	s_mov_b32 m0, s1
	v_lshl_add_u64 v[70:71], v[6:7], 0, s[20:21]
	s_mov_b32 s1, m0
	s_mov_b32 m0, s0
	s_nop 0
	global_load_lds_dwordx4 v[70:71], off
	s_mov_b32 m0, s1
	ds_read_b128 v[70:73], v2
	ds_read_b128 v[74:77], v2 offset:2048
	ds_read_b128 v[78:81], v10 offset:16384
	ds_read_b128 v[82:85], v10 offset:18432
	ds_read_b128 v[86:89], v10 offset:20480
	ds_read_b128 v[90:93], v10 offset:22528
	s_waitcnt lgkmcnt(9)
	v_mfma_f32_16x16x32_f16 v[58:61], v[42:45], v[50:53], v[58:61]
	s_waitcnt lgkmcnt(8)
	v_mfma_f32_16x16x32_f16 v[62:65], v[42:45], v[54:57], v[62:65]
	s_waitcnt lgkmcnt(7)
	v_mfma_f32_16x16x32_f16 v[66:69], v[42:45], v[94:97], v[66:69]
	s_waitcnt lgkmcnt(6)
	v_mfma_f32_16x16x32_f16 v[30:33], v[42:45], v[98:101], v[30:33]
	v_mfma_f32_16x16x32_f16 v[38:41], v[46:49], v[50:53], v[38:41]
	v_mfma_f32_16x16x32_f16 v[22:25], v[46:49], v[54:57], v[22:25]
	v_mfma_f32_16x16x32_f16 v[26:29], v[46:49], v[94:97], v[26:29]
	v_mfma_f32_16x16x32_f16 v[34:37], v[46:49], v[98:101], v[34:37]
	s_mov_b64 s[0:1], 0x22700
	v_lshl_add_u64 v[42:43], v[4:5], 0, s[0:1]
	s_mov_b32 s4, m0
	s_mov_b32 m0, s7
	s_nop 0
	global_load_lds_dwordx4 v[42:43], off
	s_mov_b32 m0, s4
	v_lshl_add_u64 v[42:43], v[6:7], 0, s[0:1]
	s_mov_b32 s0, m0
	s_mov_b32 m0, s15
	s_nop 0
	global_load_lds_dwordx4 v[42:43], off
	s_mov_b32 m0, s0
	ds_read_b128 v[42:45], v12
	ds_read_b128 v[46:49], v12 offset:2048
	ds_read_b128 v[50:53], v11 offset:16384
	ds_read_b128 v[54:57], v11 offset:18432
	ds_read_b128 v[94:97], v11 offset:20480
	ds_read_b128 v[98:101], v11 offset:22528
	s_waitcnt lgkmcnt(9)
	v_mfma_f32_16x16x32_f16 v[58:61], v[70:73], v[78:81], v[58:61]
	s_waitcnt lgkmcnt(8)
	v_mfma_f32_16x16x32_f16 v[62:65], v[70:73], v[82:85], v[62:65]
	s_waitcnt lgkmcnt(7)
	v_mfma_f32_16x16x32_f16 v[66:69], v[70:73], v[86:89], v[66:69]
	s_waitcnt lgkmcnt(6)
	v_mfma_f32_16x16x32_f16 v[30:33], v[70:73], v[90:93], v[30:33]
	v_mfma_f32_16x16x32_f16 v[38:41], v[74:77], v[78:81], v[38:41]
	v_mfma_f32_16x16x32_f16 v[22:25], v[74:77], v[82:85], v[22:25]
	v_mfma_f32_16x16x32_f16 v[26:29], v[74:77], v[86:89], v[26:29]
	v_mfma_f32_16x16x32_f16 v[34:37], v[74:77], v[90:93], v[34:37]
	s_mov_b64 s[0:1], 0x780
	s_waitcnt vmcnt(4)
	s_barrier
	v_lshl_add_u64 v[70:71], v[4:5], 0, s[0:1]
	s_mov_b32 s4, m0
	s_mov_b32 m0, s17
	s_nop 0
	global_load_lds_dwordx4 v[70:71], off
	s_mov_b32 m0, s4
	v_lshl_add_u64 v[70:71], v[6:7], 0, s[0:1]
	s_mov_b32 s0, m0
	s_mov_b32 m0, s19
	s_nop 0
	global_load_lds_dwordx4 v[70:71], off
	s_mov_b32 m0, s0
	ds_read_b128 v[70:73], v2 offset:32768
	ds_read_b128 v[74:77], v2 offset:34816
	ds_read_b128 v[78:81], v10 offset:49152
	ds_read_b128 v[82:85], v10 offset:51200
	ds_read_b128 v[86:89], v10 offset:53248
	ds_read_b128 v[90:93], v10 offset:55296
	s_waitcnt lgkmcnt(9)
	v_mfma_f32_16x16x32_f16 v[58:61], v[42:45], v[50:53], v[58:61]
	s_waitcnt lgkmcnt(8)
	v_mfma_f32_16x16x32_f16 v[62:65], v[42:45], v[54:57], v[62:65]
	s_waitcnt lgkmcnt(7)
	v_mfma_f32_16x16x32_f16 v[66:69], v[42:45], v[94:97], v[66:69]
	s_waitcnt lgkmcnt(6)
	v_mfma_f32_16x16x32_f16 v[30:33], v[42:45], v[98:101], v[30:33]
	v_mfma_f32_16x16x32_f16 v[38:41], v[46:49], v[50:53], v[38:41]
	v_mfma_f32_16x16x32_f16 v[22:25], v[46:49], v[54:57], v[22:25]
	v_mfma_f32_16x16x32_f16 v[26:29], v[46:49], v[94:97], v[26:29]
	v_mfma_f32_16x16x32_f16 v[34:37], v[46:49], v[98:101], v[34:37]
	s_mov_b64 s[0:1], 0x22780
	v_lshl_add_u64 v[4:5], v[4:5], 0, s[0:1]
	s_mov_b32 s4, m0
	s_mov_b32 m0, s2
	s_nop 0
	global_load_lds_dwordx4 v[4:5], off
	s_mov_b32 m0, s4
	v_lshl_add_u64 v[4:5], v[6:7], 0, s[0:1]
	s_mov_b32 s0, m0
	s_mov_b32 m0, s3
	s_nop 0
	global_load_lds_dwordx4 v[4:5], off
	s_mov_b32 m0, s0
	ds_read_b128 v[4:7], v12 offset:32768
	ds_read_b128 v[42:45], v12 offset:34816
	ds_read_b128 v[46:49], v11 offset:49152
	ds_read_b128 v[50:53], v11 offset:51200
	ds_read_b128 v[54:57], v11 offset:53248
	ds_read_b128 v[94:97], v11 offset:55296
	s_waitcnt lgkmcnt(9)
	v_mfma_f32_16x16x32_f16 v[58:61], v[70:73], v[78:81], v[58:61]
	s_waitcnt lgkmcnt(8)
	v_mfma_f32_16x16x32_f16 v[62:65], v[70:73], v[82:85], v[62:65]
	s_waitcnt lgkmcnt(7)
	v_mfma_f32_16x16x32_f16 v[66:69], v[70:73], v[86:89], v[66:69]
	s_waitcnt lgkmcnt(6)
	v_mfma_f32_16x16x32_f16 v[30:33], v[70:73], v[90:93], v[30:33]
	v_mfma_f32_16x16x32_f16 v[38:41], v[74:77], v[78:81], v[38:41]
	v_mfma_f32_16x16x32_f16 v[22:25], v[74:77], v[82:85], v[22:25]
	v_mfma_f32_16x16x32_f16 v[26:29], v[74:77], v[86:89], v[26:29]
	v_mfma_f32_16x16x32_f16 v[34:37], v[74:77], v[90:93], v[34:37]
	s_waitcnt vmcnt(4)
	s_barrier
	ds_read_b128 v[70:73], v14
	ds_read_b128 v[74:77], v14 offset:2048
	ds_read_b128 v[78:81], v13 offset:6144
	ds_read_b128 v[82:85], v13 offset:4096
	ds_read_b128 v[86:89], v13 offset:2048
	ds_read_b128 v[10:13], v13
	s_waitcnt lgkmcnt(9)
	v_mfma_f32_16x16x32_f16 v[58:61], v[4:7], v[46:49], v[58:61]
	s_waitcnt lgkmcnt(8)
	v_mfma_f32_16x16x32_f16 v[62:65], v[4:7], v[50:53], v[62:65]
	s_waitcnt lgkmcnt(7)
	v_mfma_f32_16x16x32_f16 v[66:69], v[4:7], v[54:57], v[66:69]
	s_waitcnt lgkmcnt(6)
	v_mfma_f32_16x16x32_f16 v[4:7], v[4:7], v[94:97], v[30:33]
	v_mfma_f32_16x16x32_f16 v[30:33], v[42:45], v[46:49], v[38:41]
	v_mfma_f32_16x16x32_f16 v[22:25], v[42:45], v[50:53], v[22:25]
	v_mfma_f32_16x16x32_f16 v[26:29], v[42:45], v[54:57], v[26:29]
	v_mfma_f32_16x16x32_f16 v[34:37], v[42:45], v[94:97], v[34:37]
	ds_read_b128 v[38:41], v16
	ds_read_b128 v[42:45], v16 offset:2048
	ds_read_b128 v[46:49], v15
	ds_read_b128 v[50:53], v15 offset:2048
	ds_read_b128 v[54:57], v15 offset:4096
	ds_read_b128 v[90:93], v15 offset:6144
	s_waitcnt lgkmcnt(6)
	v_mfma_f32_16x16x32_f16 v[58:61], v[70:73], v[10:13], v[58:61]
	v_mfma_f32_16x16x32_f16 v[62:65], v[70:73], v[86:89], v[62:65]
	v_mfma_f32_16x16x32_f16 v[66:69], v[70:73], v[82:85], v[66:69]
	v_mfma_f32_16x16x32_f16 v[4:7], v[70:73], v[78:81], v[4:7]
	v_mfma_f32_16x16x32_f16 v[10:13], v[74:77], v[10:13], v[30:33]
	v_mfma_f32_16x16x32_f16 v[22:25], v[74:77], v[86:89], v[22:25]
	v_mfma_f32_16x16x32_f16 v[26:29], v[74:77], v[82:85], v[26:29]
	v_mfma_f32_16x16x32_f16 v[30:33], v[74:77], v[78:81], v[34:37]
	s_waitcnt vmcnt(0)
	s_barrier
	s_nop 1
	ds_read_b128 v[34:37], v18 offset:6144
	ds_read_b128 v[70:73], v18 offset:4096
	ds_read_b128 v[74:77], v18 offset:2048
	ds_read_b128 v[78:81], v18
	ds_read_b128 v[82:85], v17 offset:2048
	ds_read_b128 v[14:17], v17
	s_waitcnt lgkmcnt(9)
	v_mfma_f32_16x16x32_f16 v[58:61], v[38:41], v[46:49], v[58:61]
	s_waitcnt lgkmcnt(8)
	v_mfma_f32_16x16x32_f16 v[62:65], v[38:41], v[50:53], v[62:65]
	s_waitcnt lgkmcnt(7)
	v_mfma_f32_16x16x32_f16 v[66:69], v[38:41], v[54:57], v[66:69]
	s_waitcnt lgkmcnt(6)
	v_mfma_f32_16x16x32_f16 v[4:7], v[38:41], v[90:93], v[4:7]
	v_mfma_f32_16x16x32_f16 v[10:13], v[42:45], v[46:49], v[10:13]
	v_mfma_f32_16x16x32_f16 v[22:25], v[42:45], v[50:53], v[22:25]
	v_mfma_f32_16x16x32_f16 v[26:29], v[42:45], v[54:57], v[26:29]
	v_mfma_f32_16x16x32_f16 v[30:33], v[42:45], v[90:93], v[30:33]
	ds_read_b128 v[38:41], v20
	ds_read_b128 v[42:45], v20 offset:2048
	ds_read_b128 v[46:49], v20 offset:4096
	ds_read_b128 v[50:53], v20 offset:6144
	ds_read_b128 v[54:57], v19 offset:2048
	ds_read_b128 v[18:21], v19
	v_and_b32_e32 v0, 64, v0
	s_waitcnt lgkmcnt(6)
	v_mfma_f32_16x16x32_f16 v[58:61], v[14:17], v[78:81], v[58:61]
	v_mfma_f32_16x16x32_f16 v[62:65], v[14:17], v[74:77], v[62:65]
	v_mfma_f32_16x16x32_f16 v[66:69], v[14:17], v[70:73], v[66:69]
	v_mfma_f32_16x16x32_f16 v[4:7], v[14:17], v[34:37], v[4:7]
	v_mfma_f32_16x16x32_f16 v[10:13], v[82:85], v[78:81], v[10:13]
	v_mfma_f32_16x16x32_f16 v[14:17], v[82:85], v[74:77], v[22:25]
	v_mfma_f32_16x16x32_f16 v[22:25], v[82:85], v[70:73], v[26:29]
	v_mfma_f32_16x16x32_f16 v[26:29], v[82:85], v[34:37], v[30:33]
	s_waitcnt lgkmcnt(0)
	v_mfma_f32_16x16x32_f16 v[30:33], v[18:21], v[38:41], v[58:61]
	v_mfma_f32_16x16x32_f16 v[34:37], v[18:21], v[42:45], v[62:65]
	v_mfma_f32_16x16x32_f16 v[58:61], v[18:21], v[46:49], v[66:69]
	v_mfma_f32_16x16x32_f16 v[4:7], v[18:21], v[50:53], v[4:7]
	v_mfma_f32_16x16x32_f16 v[10:13], v[54:57], v[38:41], v[10:13]
	v_mfma_f32_16x16x32_f16 v[14:17], v[54:57], v[42:45], v[14:17]
	v_mfma_f32_16x16x32_f16 v[18:21], v[54:57], v[46:49], v[22:25]
	v_mfma_f32_16x16x32_f16 v[22:25], v[54:57], v[50:53], v[26:29]
	s_lshl_b32 s0, s13, 7
	v_or3_b32 v0, s0, v0, v9
	v_lshlrev_b32_e32 v2, 2, v0
	global_load_dword v46, v2, s[8:9]
	global_load_dword v47, v2, s[8:9] offset:64
	global_load_dword v48, v2, s[8:9] offset:128
	global_load_dword v49, v2, s[8:9] offset:192
	v_and_b32_e32 v0, 12, v1
	v_or3_b32 v0, s12, v8, v0
	v_ashrrev_i32_e32 v1, 31, v0
	v_or_b32_e32 v8, 1, v0
	v_or_b32_e32 v26, 2, v0
	v_or_b32_e32 v28, 3, v0
	v_or_b32_e32 v38, 16, v0
	v_or_b32_e32 v40, 17, v0
	v_or_b32_e32 v42, 18, v0
	v_or_b32_e32 v44, 19, v0
	v_lshl_add_u64 v[2:3], s[10:11], 0, v[2:3]
	v_lshlrev_b64 v[0:1], 12, v[0:1]
	v_ashrrev_i32_e32 v9, 31, v8
	v_ashrrev_i32_e32 v27, 31, v26
	v_ashrrev_i32_e32 v29, 31, v28
	v_ashrrev_i32_e32 v39, 31, v38
	v_ashrrev_i32_e32 v41, 31, v40
	v_ashrrev_i32_e32 v43, 31, v42
	v_ashrrev_i32_e32 v45, 31, v44
	v_lshl_add_u64 v[0:1], v[2:3], 0, v[0:1]
	v_lshlrev_b64 v[8:9], 12, v[8:9]
	v_lshlrev_b64 v[26:27], 12, v[26:27]
	v_lshlrev_b64 v[28:29], 12, v[28:29]
	v_lshlrev_b64 v[38:39], 12, v[38:39]
	v_lshlrev_b64 v[40:41], 12, v[40:41]
	v_lshlrev_b64 v[42:43], 12, v[42:43]
	v_lshlrev_b64 v[44:45], 12, v[44:45]
	v_lshl_add_u64 v[8:9], v[2:3], 0, v[8:9]
	v_lshl_add_u64 v[26:27], v[2:3], 0, v[26:27]
	v_lshl_add_u64 v[28:29], v[2:3], 0, v[28:29]
	v_lshl_add_u64 v[38:39], v[2:3], 0, v[38:39]
	v_lshl_add_u64 v[40:41], v[2:3], 0, v[40:41]
	v_lshl_add_u64 v[42:43], v[2:3], 0, v[42:43]
	v_lshl_add_u64 v[2:3], v[2:3], 0, v[44:45]
	s_waitcnt vmcnt(3)
	v_add_f32_e32 v30, v46, v30
	v_add_f32_e32 v31, v46, v31
	v_add_f32_e32 v32, v46, v32
	s_waitcnt vmcnt(0)
	v_add_f32_e32 v4, v49, v4
	v_add_f32_e32 v33, v46, v33
	v_add_f32_e32 v10, v46, v10
	v_add_f32_e32 v11, v46, v11
	v_add_f32_e32 v12, v46, v12
	v_add_f32_e32 v13, v46, v13
	v_add_f32_e32 v34, v47, v34
	v_add_f32_e32 v35, v47, v35
	v_add_f32_e32 v36, v47, v36
	v_add_f32_e32 v37, v47, v37
	v_add_f32_e32 v14, v47, v14
	v_add_f32_e32 v15, v47, v15
	v_add_f32_e32 v16, v47, v16
	v_add_f32_e32 v17, v47, v17
	v_add_f32_e32 v44, v48, v58
	v_add_f32_e32 v45, v48, v59
	v_add_f32_e32 v46, v48, v60
	v_add_f32_e32 v47, v48, v61
	v_add_f32_e32 v18, v48, v18
	v_add_f32_e32 v19, v48, v19
	global_store_dword v[0:1], v30, off nt
	global_store_dword v[8:9], v31, off nt
	global_store_dword v[26:27], v32, off nt
	global_store_dword v[28:29], v33, off nt
	global_store_dword v[38:39], v10, off nt
	global_store_dword v[40:41], v11, off nt
	global_store_dword v[42:43], v12, off nt
	global_store_dword v[2:3], v13, off nt
	global_store_dword v[0:1], v34, off offset:64 nt
	global_store_dword v[8:9], v35, off offset:64 nt
	global_store_dword v[26:27], v36, off offset:64 nt
	global_store_dword v[28:29], v37, off offset:64 nt
	global_store_dword v[38:39], v14, off offset:64 nt
	global_store_dword v[40:41], v15, off offset:64 nt
	global_store_dword v[42:43], v16, off offset:64 nt
	global_store_dword v[2:3], v17, off offset:64 nt
	global_store_dword v[0:1], v44, off offset:128 nt
	global_store_dword v[8:9], v45, off offset:128 nt
	global_store_dword v[26:27], v46, off offset:128 nt
	global_store_dword v[28:29], v47, off offset:128 nt
	global_store_dword v[38:39], v18, off offset:128 nt
	global_store_dword v[40:41], v19, off offset:128 nt
	global_store_dword v[0:1], v4, off offset:192 nt
	v_add_f32_e32 v0, v49, v5
	global_store_dword v[8:9], v0, off offset:192 nt
	v_add_f32_e32 v0, v49, v6
	global_store_dword v[26:27], v0, off offset:192 nt
	v_add_f32_e32 v0, v49, v7
	global_store_dword v[28:29], v0, off offset:192 nt
	v_add_f32_e32 v0, v49, v22
	global_store_dword v[38:39], v0, off offset:192 nt
	v_add_f32_e32 v0, v49, v23
	v_add_f32_e32 v10, v48, v20
	global_store_dword v[40:41], v0, off offset:192 nt
	v_add_f32_e32 v0, v49, v24
	global_store_dword v[42:43], v10, off offset:128 nt
	v_add_f32_e32 v10, v48, v21
	global_store_dword v[42:43], v0, off offset:192 nt
	v_add_f32_e32 v0, v49, v25
	global_store_dword v[2:3], v10, off offset:128 nt
	global_store_dword v[2:3], v0, off offset:192 nt
	s_endpgm

	.amdhsa_kernel _Z12oproj_kernelPKDF16_S0_PKfPf
		.amdhsa_group_segment_fixed_size 0
		.amdhsa_private_segment_fixed_size 0
		.amdhsa_kernarg_size 32
		.amdhsa_user_sgpr_count 2
		.amdhsa_user_sgpr_dispatch_ptr 0
		.amdhsa_user_sgpr_queue_ptr 0
		.amdhsa_user_sgpr_kernarg_segment_ptr 1
		.amdhsa_user_sgpr_dispatch_id 0
		.amdhsa_user_sgpr_kernarg_preload_length 0
		.amdhsa_user_sgpr_kernarg_preload_offset 0
		.amdhsa_user_sgpr_private_segment_size 0
		.amdhsa_uses_dynamic_stack 0
		.amdhsa_enable_private_segment 0
		.amdhsa_system_sgpr_workgroup_id_x 1
		.amdhsa_system_sgpr_workgroup_id_y 0
		.amdhsa_system_sgpr_workgroup_id_z 0
		.amdhsa_system_sgpr_workgroup_info 0
		.amdhsa_system_vgpr_workitem_id 0
		.amdhsa_next_free_vgpr 108
		.amdhsa_next_free_sgpr 28
		.amdhsa_accum_offset 108
		.amdhsa_reserve_vcc 0
		.amdhsa_float_round_mode_32 0
		.amdhsa_float_round_mode_16_64 0
		.amdhsa_float_denorm_mode_32 3
		.amdhsa_float_denorm_mode_16_64 3
		.amdhsa_dx10_clamp 1
		.amdhsa_ieee_mode 1
		.amdhsa_fp16_overflow 0
		.amdhsa_tg_split 0
		.amdhsa_exception_fp_ieee_invalid_op 0
		.amdhsa_exception_fp_denorm_src 0
		.amdhsa_exception_fp_ieee_div_zero 0
		.amdhsa_exception_fp_ieee_overflow 0
		.amdhsa_exception_fp_ieee_underflow 0
		.amdhsa_exception_fp_ieee_inexact 0
		.amdhsa_exception_int_div_zero 0
	.end_amdhsa_kernel

amdhsa.kernels:
  - .agpr_count:     0
    .args:
      - .actual_access:  read_only
        .address_space:  global
        .offset:         0
        .size:           8
        .value_kind:     global_buffer
      - .actual_access:  read_only
        .address_space:  global
        .offset:         8
        .size:           8
        .value_kind:     global_buffer
      - .actual_access:  read_only
        .address_space:  global
        .offset:         16
        .size:           8
        .value_kind:     global_buffer
      - .actual_access:  read_only
        .address_space:  global
        .offset:         24
        .size:           8
        .value_kind:     global_buffer
      - .actual_access:  read_only
        .address_space:  global
        .offset:         32
        .size:           8
        .value_kind:     global_buffer
      - .actual_access:  read_only
        .address_space:  global
        .offset:         40
        .size:           8
        .value_kind:     global_buffer
      - .actual_access:  read_only
        .address_space:  global
        .offset:         48
        .size:           8
        .value_kind:     global_buffer
      - .actual_access:  read_only
        .address_space:  global
        .offset:         56
        .size:           8
        .value_kind:     global_buffer
      - .actual_access:  write_only
        .address_space:  global
        .offset:         64
        .size:           8
        .value_kind:     global_buffer
      - .actual_access:  write_only
        .address_space:  global
        .offset:         72
        .size:           8
        .value_kind:     global_buffer
      - .actual_access:  write_only
        .address_space:  global
        .offset:         80
        .size:           8
        .value_kind:     global_buffer
      - .actual_access:  write_only
        .address_space:  global
        .offset:         88
        .size:           8
        .value_kind:     global_buffer
      - .actual_access:  write_only
        .address_space:  global
        .offset:         96
        .size:           8
        .value_kind:     global_buffer
    .group_segment_fixed_size: 80
    .kernarg_segment_align: 8
    .kernarg_segment_size: 104
    .language:       OpenCL C
    .language_version:
      - 2
      - 0
    .max_flat_workgroup_size: 256
    .name:           _Z11prep_kernelPKfS0_S0_PKiS0_S0_S0_S0_PDF16_S3_S3_S3_Pi
    .private_segment_fixed_size: 0
    .sgpr_count:     43
    .sgpr_spill_count: 0
    .symbol:         _Z11prep_kernelPKfS0_S0_PKiS0_S0_S0_S0_PDF16_S3_S3_S3_Pi.kd
    .uniform_work_group_size: 1
    .uses_dynamic_stack: false
    .vgpr_count:     64
    .vgpr_spill_count: 0
    .wavefront_size: 64
  - .agpr_count:     0
    .args:
      - .address_space:  global
        .offset:         0
        .size:           8
        .value_kind:     global_buffer
      - .address_space:  global
        .offset:         8
        .size:           8
        .value_kind:     global_buffer
      - .address_space:  global
        .offset:         16
        .size:           8
        .value_kind:     global_buffer
      - .address_space:  global
        .offset:         24
        .size:           8
        .value_kind:     global_buffer
      - .actual_access:  read_only
        .address_space:  global
        .offset:         32
        .size:           8
        .value_kind:     global_buffer
      - .actual_access:  read_only
        .address_space:  global
        .offset:         40
        .size:           8
        .value_kind:     global_buffer
      - .actual_access:  read_only
        .address_space:  global
        .offset:         48
        .size:           8
        .value_kind:     global_buffer
      - .actual_access:  read_only
        .address_space:  global
        .offset:         56
        .size:           8
        .value_kind:     global_buffer
      - .actual_access:  read_only
        .address_space:  global
        .offset:         64
        .size:           8
        .value_kind:     global_buffer
      - .actual_access:  read_only
        .address_space:  global
        .offset:         72
        .size:           8
        .value_kind:     global_buffer
      - .actual_access:  write_only
        .address_space:  global
        .offset:         80
        .size:           8
        .value_kind:     global_buffer
      - .actual_access:  write_only
        .address_space:  global
        .offset:         88
        .size:           8
        .value_kind:     global_buffer
      - .actual_access:  write_only
        .address_space:  global
        .offset:         96
        .size:           8
        .value_kind:     global_buffer
    .group_segment_fixed_size: 28672
    .kernarg_segment_align: 8
    .kernarg_segment_size: 104
    .language:       OpenCL C
    .language_version:
      - 2
      - 0
    .max_flat_workgroup_size: 512
    .name:           _Z11proj_kernelPKDF16_S0_S0_S0_PKiPKfS4_S4_S4_S4_PDF16_S5_S5_
    .private_segment_fixed_size: 0
    .sgpr_count:     66
    .sgpr_spill_count: 0
    .symbol:         _Z11proj_kernelPKDF16_S0_S0_S0_PKiPKfS4_S4_S4_S4_PDF16_S5_S5_.kd
    .uniform_work_group_size: 1
    .uses_dynamic_stack: false
    .vgpr_count:     217
    .vgpr_spill_count: 0
    .wavefront_size: 64
  - .agpr_count:     0
    .args:
      - .actual_access:  read_only
        .address_space:  global
        .offset:         0
        .size:           8
        .value_kind:     global_buffer
      - .address_space:  global
        .offset:         8
        .size:           8
        .value_kind:     global_buffer
      - .address_space:  global
        .offset:         16
        .size:           8
        .value_kind:     global_buffer
      - .actual_access:  read_only
        .address_space:  global
        .offset:         24
        .size:           8
        .value_kind:     global_buffer
      - .actual_access:  write_only
        .address_space:  global
        .offset:         32
        .size:           8
        .value_kind:     global_buffer
      - .actual_access:  read_only
        .address_space:  global
        .offset:         40
        .size:           8
        .value_kind:     global_buffer
      - .actual_access:  write_only
        .address_space:  global
        .offset:         48
        .size:           8
        .value_kind:     global_buffer
    .group_segment_fixed_size: 0
    .kernarg_segment_align: 8
    .kernarg_segment_size: 56
    .language:       OpenCL C
    .language_version:
      - 2
      - 0
    .max_flat_workgroup_size: 512
    .name:           _Z11attn_kernelPKDF16_S0_S0_PKiPDF16_PKfS3_
    .private_segment_fixed_size: 0
    .sgpr_count:     100
    .sgpr_spill_count: 0
    .symbol:         _Z11attn_kernelPKDF16_S0_S0_PKiPDF16_PKfS3_.kd
    .uniform_work_group_size: 1
    .uses_dynamic_stack: false
    .vgpr_count:     204
    .vgpr_spill_count: 0
    .wavefront_size: 64
  - .agpr_count:     0
    .args:
      - .address_space:  global
        .offset:         0
        .size:           8
        .value_kind:     global_buffer
      - .address_space:  global
        .offset:         8
        .size:           8
        .value_kind:     global_buffer
      - .actual_access:  read_only
        .address_space:  global
        .offset:         16
        .size:           8
        .value_kind:     global_buffer
      - .actual_access:  write_only
        .address_space:  global
        .offset:         24
        .size:           8
        .value_kind:     global_buffer
    .group_segment_fixed_size: 0
    .kernarg_segment_align: 8
    .kernarg_segment_size: 32
    .language:       OpenCL C
    .language_version:
      - 2
      - 0
    .max_flat_workgroup_size: 512
    .name:           _Z12oproj_kernelPKDF16_S0_PKfPf
    .private_segment_fixed_size: 0
    .sgpr_count:     34
    .sgpr_spill_count: 0
    .symbol:         _Z12oproj_kernelPKDF16_S0_PKfPf.kd
    .uniform_work_group_size: 1
    .uses_dynamic_stack: false
    .vgpr_count:     108
    .vgpr_spill_count: 0
    .wavefront_size: 64
